# v59 + conv: rsqrt of the variance taken once on the reduced vector before the broadcast (8 fma + 8 rsq fewer per step)
# speedup vs baseline: 1.0069x; 1.0015x over previous
; __device__ __forceinline__ void ph_conv2(const Params& p, int l, LAS unsigned char* lds, const int wvid) {
;     ...
;             for (int i = 0; i < 38; ++i) x[i] = G[(tl + i) * 256 + c];
; #pragma unroll
;             for (int o = 0; o < 8; ++o) { float acc = cb;
; #pragma unroll
;                 for (int w = 0; w < 31; ++w) acc += wv[w] * x[o + w];
.LBB0_456:
	ds_read2st64_b32 v[40:41], v0 offset1:4
	ds_read2st64_b32 v[38:39], v0 offset0:8 offset1:12
	ds_read2st64_b32 v[36:37], v0 offset0:16 offset1:20
	ds_read2st64_b32 v[34:35], v0 offset0:24 offset1:28
	ds_read2st64_b32 v[32:33], v0 offset0:32 offset1:36
	ds_read2st64_b32 v[30:31], v0 offset0:40 offset1:44
	ds_read2st64_b32 v[28:29], v0 offset0:48 offset1:52
	ds_read2st64_b32 v[26:27], v0 offset0:56 offset1:60
	ds_read2st64_b32 v[24:25], v0 offset0:64 offset1:68
	ds_read2st64_b32 v[22:23], v0 offset0:72 offset1:76
	ds_read2st64_b32 v[20:21], v0 offset0:80 offset1:84
	ds_read2st64_b32 v[18:19], v0 offset0:88 offset1:92
	ds_read2st64_b32 v[16:17], v0 offset0:96 offset1:100
	ds_read2st64_b32 v[14:15], v0 offset0:104 offset1:108
	ds_read2st64_b32 v[12:13], v0 offset0:112 offset1:116
	ds_read2st64_b32 v[10:11], v0 offset0:120 offset1:124
	ds_read2st64_b32 v[8:9], v0 offset0:128 offset1:132
	ds_read2st64_b32 v[6:7], v0 offset0:136 offset1:140
	ds_read2st64_b32 v[4:5], v0 offset0:144 offset1:148
	s_waitcnt lgkmcnt(15)
	v_fma_f32 v120, v60, v40, v55
	v_fmac_f32_e32 v120, v61, v41
	s_waitcnt lgkmcnt(15)
	v_fmac_f32_e32 v120, v62, v38
	v_fmac_f32_e32 v120, v63, v39
	s_waitcnt lgkmcnt(15)
	v_fmac_f32_e32 v120, v64, v36
	v_fmac_f32_e32 v120, v65, v37
	s_waitcnt lgkmcnt(15)
	v_fmac_f32_e32 v120, v66, v34
	v_fmac_f32_e32 v120, v67, v35
	s_waitcnt lgkmcnt(14)
	v_fmac_f32_e32 v120, v68, v32
	v_fmac_f32_e32 v120, v69, v33
	s_waitcnt lgkmcnt(13)
	v_fmac_f32_e32 v120, v70, v30
	v_fmac_f32_e32 v120, v71, v31
	s_waitcnt lgkmcnt(12)
	v_fmac_f32_e32 v120, v72, v28
	v_fmac_f32_e32 v120, v73, v29
	s_waitcnt lgkmcnt(11)
	v_fmac_f32_e32 v120, v74, v26
	v_fmac_f32_e32 v120, v75, v27
	s_waitcnt lgkmcnt(10)
	v_fmac_f32_e32 v120, v76, v24
	v_fmac_f32_e32 v120, v77, v25
	s_waitcnt lgkmcnt(9)
	v_fmac_f32_e32 v120, v78, v22
	v_fmac_f32_e32 v120, v79, v23
	s_waitcnt lgkmcnt(8)
	v_fmac_f32_e32 v120, v80, v20
	v_fmac_f32_e32 v120, v81, v21
	s_waitcnt lgkmcnt(7)
	v_fmac_f32_e32 v120, v82, v18
	v_fmac_f32_e32 v120, v83, v19
	s_waitcnt lgkmcnt(6)
	v_fmac_f32_e32 v120, v84, v16
	v_fmac_f32_e32 v120, v85, v17
	s_waitcnt lgkmcnt(5)
	v_fmac_f32_e32 v120, v86, v14
	v_fmac_f32_e32 v120, v87, v15
	s_waitcnt lgkmcnt(4)
	v_fmac_f32_e32 v120, v88, v12
	v_fmac_f32_e32 v120, v89, v13
	s_waitcnt lgkmcnt(3)
	v_fmac_f32_e32 v120, v90, v10
	v_fma_f32 v121, v60, v41, v55
	v_fmac_f32_e32 v121, v61, v38
	v_fmac_f32_e32 v121, v62, v39
	v_fmac_f32_e32 v121, v63, v36
	v_fmac_f32_e32 v121, v64, v37
	v_fmac_f32_e32 v121, v65, v34
	v_fmac_f32_e32 v121, v66, v35
	v_fmac_f32_e32 v121, v67, v32
	v_fmac_f32_e32 v121, v68, v33
	v_fmac_f32_e32 v121, v69, v30
	v_fmac_f32_e32 v121, v70, v31
	v_fmac_f32_e32 v121, v71, v28
	v_fmac_f32_e32 v121, v72, v29
	v_fmac_f32_e32 v121, v73, v26
	v_fmac_f32_e32 v121, v74, v27
	v_fmac_f32_e32 v121, v75, v24
	v_fmac_f32_e32 v121, v76, v25
	v_fmac_f32_e32 v121, v77, v22
	v_fmac_f32_e32 v121, v78, v23
	v_fmac_f32_e32 v121, v79, v20
	v_fmac_f32_e32 v121, v80, v21
	v_fmac_f32_e32 v121, v81, v18
	v_fmac_f32_e32 v121, v82, v19
	v_fmac_f32_e32 v121, v83, v16
	v_fmac_f32_e32 v121, v84, v17
	v_fmac_f32_e32 v121, v85, v14
	v_fmac_f32_e32 v121, v86, v15
	v_fmac_f32_e32 v121, v87, v12
	v_fmac_f32_e32 v121, v88, v13
	v_fmac_f32_e32 v121, v89, v10
	v_fmac_f32_e32 v121, v90, v11
	v_fma_f32 v122, v60, v38, v55
	v_fmac_f32_e32 v122, v61, v39
	v_fmac_f32_e32 v122, v62, v36
	v_fmac_f32_e32 v122, v63, v37
	v_fmac_f32_e32 v122, v64, v34
	v_fmac_f32_e32 v122, v65, v35
	v_fmac_f32_e32 v122, v66, v32
	v_fmac_f32_e32 v122, v67, v33
	v_fmac_f32_e32 v122, v68, v30
	v_fmac_f32_e32 v122, v69, v31
	v_fmac_f32_e32 v122, v70, v28
	v_fmac_f32_e32 v122, v71, v29
	v_fmac_f32_e32 v122, v72, v26
	v_fmac_f32_e32 v122, v73, v27
	v_fmac_f32_e32 v122, v74, v24
	v_fmac_f32_e32 v122, v75, v25
	v_fmac_f32_e32 v122, v76, v22
	v_fmac_f32_e32 v122, v77, v23
	v_fmac_f32_e32 v122, v78, v20
	v_fmac_f32_e32 v122, v79, v21
	v_fmac_f32_e32 v122, v80, v18
	v_fmac_f32_e32 v122, v81, v19
	v_fmac_f32_e32 v122, v82, v16
	v_fmac_f32_e32 v122, v83, v17
	v_fmac_f32_e32 v122, v84, v14
	v_fmac_f32_e32 v122, v85, v15
	v_fmac_f32_e32 v122, v86, v12
	v_fmac_f32_e32 v122, v87, v13
	v_fmac_f32_e32 v122, v88, v10
	v_fmac_f32_e32 v122, v89, v11
	s_waitcnt lgkmcnt(2)
	v_fmac_f32_e32 v122, v90, v8
	v_fma_f32 v123, v60, v39, v55
	v_fmac_f32_e32 v123, v61, v36
	v_fmac_f32_e32 v123, v62, v37
	v_fmac_f32_e32 v123, v63, v34
	v_fmac_f32_e32 v123, v64, v35
	v_fmac_f32_e32 v123, v65, v32
	v_fmac_f32_e32 v123, v66, v33
	v_fmac_f32_e32 v123, v67, v30
	v_fmac_f32_e32 v123, v68, v31
	v_fmac_f32_e32 v123, v69, v28
	v_fmac_f32_e32 v123, v70, v29
	v_fmac_f32_e32 v123, v71, v26
	v_fmac_f32_e32 v123, v72, v27
	v_fmac_f32_e32 v123, v73, v24
	v_fmac_f32_e32 v123, v74, v25
	v_fmac_f32_e32 v123, v75, v22
	v_fmac_f32_e32 v123, v76, v23
	v_fmac_f32_e32 v123, v77, v20
	v_fmac_f32_e32 v123, v78, v21
	v_fmac_f32_e32 v123, v79, v18
	v_fmac_f32_e32 v123, v80, v19
	v_fmac_f32_e32 v123, v81, v16
	v_fmac_f32_e32 v123, v82, v17
	v_fmac_f32_e32 v123, v83, v14
	v_fmac_f32_e32 v123, v84, v15
	v_fmac_f32_e32 v123, v85, v12
	v_fmac_f32_e32 v123, v86, v13
	v_fmac_f32_e32 v123, v87, v10
	v_fmac_f32_e32 v123, v88, v11
	v_fmac_f32_e32 v123, v89, v8
	v_fmac_f32_e32 v123, v90, v9
	v_fma_f32 v124, v60, v36, v55
	v_fmac_f32_e32 v124, v61, v37
	v_fmac_f32_e32 v124, v62, v34
	v_fmac_f32_e32 v124, v63, v35
	v_fmac_f32_e32 v124, v64, v32
	v_fmac_f32_e32 v124, v65, v33
	v_fmac_f32_e32 v124, v66, v30
	v_fmac_f32_e32 v124, v67, v31
	v_fmac_f32_e32 v124, v68, v28
	v_fmac_f32_e32 v124, v69, v29
	v_fmac_f32_e32 v124, v70, v26
	v_fmac_f32_e32 v124, v71, v27
	v_fmac_f32_e32 v124, v72, v24
	v_fmac_f32_e32 v124, v73, v25
	v_fmac_f32_e32 v124, v74, v22
	v_fmac_f32_e32 v124, v75, v23
	v_fmac_f32_e32 v124, v76, v20
	v_fmac_f32_e32 v124, v77, v21
	v_fmac_f32_e32 v124, v78, v18
	v_fmac_f32_e32 v124, v79, v19
	v_fmac_f32_e32 v124, v80, v16
	v_fmac_f32_e32 v124, v81, v17
	v_fmac_f32_e32 v124, v82, v14
	v_fmac_f32_e32 v124, v83, v15
	v_fmac_f32_e32 v124, v84, v12
	v_fmac_f32_e32 v124, v85, v13
	v_fmac_f32_e32 v124, v86, v10
	v_fmac_f32_e32 v124, v87, v11
	v_fmac_f32_e32 v124, v88, v8
	v_fmac_f32_e32 v124, v89, v9
	s_waitcnt lgkmcnt(1)
; __device__ __forceinline__ void ph_conv2(const Params& p, int l, LAS unsigned char* lds, const int wvid) {
;     ...
;             for (int o = 0; o < 8; ++o) { float acc = cb;
; #pragma unroll
;                 for (int w = 0; w < 31; ++w) acc += wv[w] * x[o + w];
;                 const float mean = wave_sum(acc) * (1.f / 64.f); const float dv = acc - mean; const float var = wave_sum(dv * dv) * (1.f / 64.f);
	v_fmac_f32_e32 v124, v90, v6
	v_fma_f32 v125, v60, v37, v55
	v_fmac_f32_e32 v125, v61, v34
	v_fmac_f32_e32 v125, v62, v35
	v_fmac_f32_e32 v125, v63, v32
	v_fmac_f32_e32 v125, v64, v33
	v_fmac_f32_e32 v125, v65, v30
	v_fmac_f32_e32 v125, v66, v31
	v_fmac_f32_e32 v125, v67, v28
	v_fmac_f32_e32 v125, v68, v29
	v_fmac_f32_e32 v125, v69, v26
	v_fmac_f32_e32 v125, v70, v27
	v_fmac_f32_e32 v125, v71, v24
	v_fmac_f32_e32 v125, v72, v25
	v_fmac_f32_e32 v125, v73, v22
	v_fmac_f32_e32 v125, v74, v23
	v_fmac_f32_e32 v125, v75, v20
	v_fmac_f32_e32 v125, v76, v21
	v_fmac_f32_e32 v125, v77, v18
	v_fmac_f32_e32 v125, v78, v19
	v_fmac_f32_e32 v125, v79, v16
	v_fmac_f32_e32 v125, v80, v17
	v_fmac_f32_e32 v125, v81, v14
	v_fmac_f32_e32 v125, v82, v15
	v_fmac_f32_e32 v125, v83, v12
	v_fmac_f32_e32 v125, v84, v13
	v_fmac_f32_e32 v125, v85, v10
	v_fmac_f32_e32 v125, v86, v11
	v_fmac_f32_e32 v125, v87, v8
	v_fmac_f32_e32 v125, v88, v9
	v_fmac_f32_e32 v125, v89, v6
	v_fmac_f32_e32 v125, v90, v7
	v_fma_f32 v126, v60, v34, v55
	v_fmac_f32_e32 v126, v61, v35
	v_fmac_f32_e32 v126, v62, v32
	v_fmac_f32_e32 v126, v63, v33
	v_fmac_f32_e32 v126, v64, v30
	v_fmac_f32_e32 v126, v65, v31
	v_fmac_f32_e32 v126, v66, v28
	v_fmac_f32_e32 v126, v67, v29
	v_fmac_f32_e32 v126, v68, v26
	v_fmac_f32_e32 v126, v69, v27
	v_fmac_f32_e32 v126, v70, v24
	v_fmac_f32_e32 v126, v71, v25
	v_fmac_f32_e32 v126, v72, v22
	v_fmac_f32_e32 v126, v73, v23
	v_fmac_f32_e32 v126, v74, v20
	v_fmac_f32_e32 v126, v75, v21
	v_fmac_f32_e32 v126, v76, v18
	v_fmac_f32_e32 v126, v77, v19
	v_fmac_f32_e32 v126, v78, v16
	v_fmac_f32_e32 v126, v79, v17
	v_fmac_f32_e32 v126, v80, v14
	v_fmac_f32_e32 v126, v81, v15
	v_fmac_f32_e32 v126, v82, v12
	v_fmac_f32_e32 v126, v83, v13
	v_fmac_f32_e32 v126, v84, v10
	v_fmac_f32_e32 v126, v85, v11
	v_fmac_f32_e32 v126, v86, v8
	v_fmac_f32_e32 v126, v87, v9
	v_fmac_f32_e32 v126, v88, v6
	v_fmac_f32_e32 v126, v89, v7
	s_waitcnt lgkmcnt(0)
	v_fmac_f32_e32 v126, v90, v4
	v_fma_f32 v127, v60, v35, v55
	v_fmac_f32_e32 v127, v61, v32
	v_fmac_f32_e32 v127, v62, v33
	v_fmac_f32_e32 v127, v63, v30
	v_fmac_f32_e32 v127, v64, v31
	v_fmac_f32_e32 v127, v65, v28
	v_fmac_f32_e32 v127, v66, v29
	v_fmac_f32_e32 v127, v67, v26
	v_fmac_f32_e32 v127, v68, v27
	v_fmac_f32_e32 v127, v69, v24
	v_fmac_f32_e32 v127, v70, v25
	v_fmac_f32_e32 v127, v71, v22
	v_fmac_f32_e32 v127, v72, v23
	v_fmac_f32_e32 v127, v73, v20
	v_fmac_f32_e32 v127, v74, v21
	v_fmac_f32_e32 v127, v75, v18
	v_fmac_f32_e32 v127, v76, v19
	v_fmac_f32_e32 v127, v77, v16
	v_fmac_f32_e32 v127, v78, v17
	v_fmac_f32_e32 v127, v79, v14
	v_fmac_f32_e32 v127, v80, v15
	v_fmac_f32_e32 v127, v81, v12
	v_fmac_f32_e32 v127, v82, v13
	v_fmac_f32_e32 v127, v83, v10
	v_fmac_f32_e32 v127, v84, v11
	v_fmac_f32_e32 v127, v85, v8
	v_fmac_f32_e32 v127, v86, v9
	v_fmac_f32_e32 v127, v87, v6
	v_fmac_f32_e32 v127, v88, v7
	v_fmac_f32_e32 v127, v89, v4
	v_fmac_f32_e32 v127, v90, v5
	s_mov_b32 vcc_lo, 0x5a5a5a5a
	s_mov_b32 vcc_hi, 0x5a5a5a5a
	v_cndmask_b32_e32 v136, v121, v120, vcc
	v_cndmask_b32_e32 v137, v123, v122, vcc
	v_cndmask_b32_e32 v138, v125, v124, vcc
	v_cndmask_b32_e32 v139, v127, v126, vcc
	v_cndmask_b32_e32 v140, v120, v121, vcc
	v_cndmask_b32_e32 v141, v122, v123, vcc
	v_cndmask_b32_e32 v142, v124, v125, vcc
	v_cndmask_b32_e32 v143, v126, v127, vcc
	v_add_f32_dpp v144, v136, v140 quad_perm:[1,0,3,2] row_mask:0xf bank_mask:0xf
	v_add_f32_dpp v145, v137, v141 quad_perm:[1,0,3,2] row_mask:0xf bank_mask:0xf
	v_add_f32_dpp v146, v138, v142 quad_perm:[1,0,3,2] row_mask:0xf bank_mask:0xf
	v_add_f32_dpp v147, v139, v143 quad_perm:[1,0,3,2] row_mask:0xf bank_mask:0xf
	s_mov_b32 vcc_lo, 0x3c3c3c3c
	s_mov_b32 vcc_hi, 0x3c3c3c3c
	v_cndmask_b32_e32 v148, v145, v144, vcc
	v_cndmask_b32_e32 v149, v147, v146, vcc
	v_cndmask_b32_e32 v150, v144, v145, vcc
	v_cndmask_b32_e32 v151, v146, v147, vcc
	s_nop 0
	v_add_f32_dpp v136, v148, v150 quad_perm:[2,3,0,1] row_mask:0xf bank_mask:0xf
	v_add_f32_dpp v137, v149, v151 quad_perm:[2,3,0,1] row_mask:0xf bank_mask:0xf
	s_mov_b32 vcc_lo, 0xff00ff00
	s_mov_b32 vcc_hi, 0xff00ff00
	v_cndmask_b32_e32 v138, v137, v136, vcc
	v_cndmask_b32_e32 v139, v136, v137, vcc
	s_nop 1
	v_add_f32_dpp v140, v138, v139 row_ror:8 row_mask:0xf bank_mask:0xf
	s_nop 1
	v_add_f32_dpp v141, v140, v140 row_half_mirror row_mask:0xf bank_mask:0xf
	v_mov_b32_e32 v142, v141
	s_nop 1
	v_permlane16_swap_b32_e32 v141, v142
	v_add_f32_e32 v143, v141, v142
	v_mov_b32_e32 v144, v143
	s_nop 1
	v_permlane32_swap_b32_e32 v143, v144
	v_add_f32_e32 v145, v143, v144
	s_nop 0
	v_readlane_b32 s24, v145, 0
	v_readlane_b32 s25, v145, 1
	v_readlane_b32 s26, v145, 2
	v_readlane_b32 s27, v145, 3
	v_readlane_b32 s28, v145, 8
	v_readlane_b32 s29, v145, 9
	v_readlane_b32 s30, v145, 10
	v_readlane_b32 s31, v145, 11
; __device__ __forceinline__ bf16_t f2bf(float f) { unsigned u = __float_as_uint(f); u += 0x7FFFu + ((u >> 16) & 1u); return (bf16_t)(u >> 16); }
; __device__ __forceinline__ float frsq(float x) { return __builtin_amdgcn_rsqf(x); }
; __device__ __forceinline__ float sigmoidf_(float x) { return frcp(1.0f + __expf(-x)); }
; __device__ __forceinline__ void ph_conv2(const Params& p, int l, LAS unsigned char* lds, const int wvid) {
;     ...
;                 const float mean = wave_sum(acc) * (1.f / 64.f); const float dv = acc - mean; const float var = wave_sum(dv * dv) * (1.f / 64.f);
;                 const float y = dv * frsq(var + 1e-5f) * gg + gb;
;                 const int tg = t0 + tl + o;
;                 if (tg < LT) MIX[((size_t)b * LT + tg) * D + M_D + c] = f2bf(y * sigmoidf_(y)); }
	v_fmac_f32_e32 v120, s24, v214
	v_fmac_f32_e32 v121, s25, v214
	v_fmac_f32_e32 v122, s26, v214
	v_fmac_f32_e32 v123, s27, v214
	v_fmac_f32_e32 v124, s28, v214
	v_fmac_f32_e32 v125, s29, v214
	v_fmac_f32_e32 v126, s30, v214
	v_fmac_f32_e32 v127, s31, v214
	v_mul_f32_e32 v128, v120, v120
	v_mul_f32_e32 v129, v121, v121
	v_mul_f32_e32 v130, v122, v122
	v_mul_f32_e32 v131, v123, v123
	v_mul_f32_e32 v132, v124, v124
	v_mul_f32_e32 v133, v125, v125
	v_mul_f32_e32 v134, v126, v126
	v_mul_f32_e32 v135, v127, v127
	s_mov_b32 vcc_lo, 0x5a5a5a5a
	s_mov_b32 vcc_hi, 0x5a5a5a5a
	v_cndmask_b32_e32 v136, v129, v128, vcc
	v_cndmask_b32_e32 v137, v131, v130, vcc
	v_cndmask_b32_e32 v138, v133, v132, vcc
	v_cndmask_b32_e32 v139, v135, v134, vcc
	v_cndmask_b32_e32 v140, v128, v129, vcc
	v_cndmask_b32_e32 v141, v130, v131, vcc
	v_cndmask_b32_e32 v142, v132, v133, vcc
	v_cndmask_b32_e32 v143, v134, v135, vcc
	v_add_f32_dpp v144, v136, v140 quad_perm:[1,0,3,2] row_mask:0xf bank_mask:0xf
	v_add_f32_dpp v145, v137, v141 quad_perm:[1,0,3,2] row_mask:0xf bank_mask:0xf
	v_add_f32_dpp v146, v138, v142 quad_perm:[1,0,3,2] row_mask:0xf bank_mask:0xf
	v_add_f32_dpp v147, v139, v143 quad_perm:[1,0,3,2] row_mask:0xf bank_mask:0xf
	s_mov_b32 vcc_lo, 0x3c3c3c3c
	s_mov_b32 vcc_hi, 0x3c3c3c3c
	v_cndmask_b32_e32 v148, v145, v144, vcc
	v_cndmask_b32_e32 v149, v147, v146, vcc
	v_cndmask_b32_e32 v150, v144, v145, vcc
	v_cndmask_b32_e32 v151, v146, v147, vcc
	s_nop 0
	v_add_f32_dpp v136, v148, v150 quad_perm:[2,3,0,1] row_mask:0xf bank_mask:0xf
	v_add_f32_dpp v137, v149, v151 quad_perm:[2,3,0,1] row_mask:0xf bank_mask:0xf
	s_mov_b32 vcc_lo, 0xff00ff00
	s_mov_b32 vcc_hi, 0xff00ff00
	v_cndmask_b32_e32 v138, v137, v136, vcc
	v_cndmask_b32_e32 v139, v136, v137, vcc
	s_nop 1
	v_add_f32_dpp v140, v138, v139 row_ror:8 row_mask:0xf bank_mask:0xf
	s_nop 1
	v_add_f32_dpp v141, v140, v140 row_half_mirror row_mask:0xf bank_mask:0xf
	v_mov_b32_e32 v142, v141
	s_nop 1
	v_permlane16_swap_b32_e32 v141, v142
	v_add_f32_e32 v143, v141, v142
	v_mov_b32_e32 v144, v143
	s_nop 1
	v_permlane32_swap_b32_e32 v143, v144
	v_add_f32_e32 v145, v143, v144
	v_fma_f32 v145, v145, v215, v204
	v_rsq_f32_e32 v145, v145
	s_nop 0
	v_readlane_b32 s24, v145, 0
	v_readlane_b32 s25, v145, 1
	v_readlane_b32 s26, v145, 2
	v_readlane_b32 s27, v145, 3
	v_readlane_b32 s28, v145, 8
	v_readlane_b32 s29, v145, 9
	v_readlane_b32 s30, v145, 10
	v_readlane_b32 s31, v145, 11
	v_mul_f32_e32 v120, s24, v120
	v_mul_f32_e32 v121, s25, v121
	v_mul_f32_e32 v122, s26, v122
	v_mul_f32_e32 v123, s27, v123
	v_mul_f32_e32 v124, s28, v124
	v_mul_f32_e32 v125, s29, v125
	v_mul_f32_e32 v126, s30, v126
	v_mul_f32_e32 v127, s31, v127
	v_fma_f32 v120, v58, v120, v59
	v_fma_f32 v121, v58, v121, v59
	v_fma_f32 v122, v58, v122, v59
	v_fma_f32 v123, v58, v123, v59
	v_fma_f32 v124, v58, v124, v59
	v_fma_f32 v125, v58, v125, v59
	v_fma_f32 v126, v58, v126, v59
	v_fma_f32 v127, v58, v127, v59
	v_mul_f32_e32 v128, 0xbfb8aa3b, v120
	v_mul_f32_e32 v129, 0xbfb8aa3b, v121
	v_mul_f32_e32 v130, 0xbfb8aa3b, v122
	v_mul_f32_e32 v131, 0xbfb8aa3b, v123
	v_mul_f32_e32 v132, 0xbfb8aa3b, v124
	v_mul_f32_e32 v133, 0xbfb8aa3b, v125
	v_mul_f32_e32 v134, 0xbfb8aa3b, v126
	v_mul_f32_e32 v135, 0xbfb8aa3b, v127
	v_exp_f32_e32 v128, v128
	v_exp_f32_e32 v129, v129
	v_exp_f32_e32 v130, v130
	v_exp_f32_e32 v131, v131
	v_exp_f32_e32 v132, v132
	v_exp_f32_e32 v133, v133
	v_exp_f32_e32 v134, v134
	v_exp_f32_e32 v135, v135
	v_add_f32_e32 v128, 1.0, v128
	v_add_f32_e32 v129, 1.0, v129
	v_add_f32_e32 v130, 1.0, v130
	v_add_f32_e32 v131, 1.0, v131
	v_add_f32_e32 v132, 1.0, v132
	v_add_f32_e32 v133, 1.0, v133
	v_add_f32_e32 v134, 1.0, v134
	v_add_f32_e32 v135, 1.0, v135
	v_rcp_f32_e32 v128, v128
	v_rcp_f32_e32 v129, v129
	v_rcp_f32_e32 v130, v130
	v_rcp_f32_e32 v131, v131
	v_rcp_f32_e32 v132, v132
	v_rcp_f32_e32 v133, v133
	v_rcp_f32_e32 v134, v134
	v_rcp_f32_e32 v135, v135
	v_mul_f32_e32 v120, v120, v128
	v_mul_f32_e32 v121, v121, v129
	v_mul_f32_e32 v122, v122, v130
	v_mul_f32_e32 v123, v123, v131
	v_mul_f32_e32 v124, v124, v132
	v_mul_f32_e32 v125, v125, v133
	v_mul_f32_e32 v126, v126, v134
	v_mul_f32_e32 v127, v127, v135
	v_cvt_pk_bf16_f32 v120, v120, v120
	v_cvt_pk_bf16_f32 v121, v121, v121
	v_cvt_pk_bf16_f32 v122, v122, v122
	v_cvt_pk_bf16_f32 v123, v123, v123
	v_cvt_pk_bf16_f32 v124, v124, v124
	v_cvt_pk_bf16_f32 v125, v125, v125
	v_cvt_pk_bf16_f32 v126, v126, v126
	v_cvt_pk_bf16_f32 v127, v127, v127
	v_readfirstlane_b32 s26, v2
	s_mov_b64 s[28:29], 0x1000
	v_mov_b32_e32 v4, v2
	v_ashrrev_i32_e32 v5, 31, v4
	v_lshl_add_u64 v[4:5], s[6:7], 0, v[4:5]
	v_lshlrev_b64 v[4:5], 11, v[4:5]
	v_lshl_add_u64 v[4:5], v[56:57], 0, v[4:5]
	s_add_i32 s27, s26, 0
	s_cmp_lt_i32 s27, s33
	s_cbranch_scc0 .Lcv_st0
	global_store_short v[4:5], v120, off
